# grid barrier: acquire invalidate issued at arrival; all workgroups poll one monotonic top counter (no per-XCD generation hop)
# speedup vs baseline: 1.0219x; 1.0219x over previous
.LBB0_101:
	s_mov_b64 s[4:5], exec
	v_readlane_b32 s2, v235, 9
	s_lshl_b32 s2, s2, 8
	v_readlane_b32 s6, v235, 7
	v_mbcnt_lo_u32_b32 v1, s4, 0
	v_readlane_b32 s7, v235, 8
	s_add_u32 s2, s6, s2
	v_mbcnt_hi_u32_b32 v1, s5, v1
	s_addc_u32 s3, s7, 0
	v_cmp_eq_u32_e32 vcc, 0, v1
	s_and_saveexec_b64 s[6:7], vcc
	s_cbranch_execz .LBB0_103
	s_bcnt1_i32_b64 s4, s[4:5]
	v_mov_b32_e32 v3, 0x1000
	v_mov_b32_e32 v4, s4
	global_atomic_add v3, v3, v4, s[2:3] offset:1024 sc0
	buffer_inv sc1
.LBB0_103:
	s_or_b64 exec, exec, s[6:7]
	v_cvt_f32_u32_e32 v4, v2
	s_waitcnt vmcnt(1)
	v_readfirstlane_b32 s4, v3
	v_sub_u32_e32 v3, 0, v2
	v_rcp_iflag_f32_e32 v4, v4
	v_add_u32_e32 v5, s4, v1
	v_mul_f32_e32 v4, 0x4f7ffffe, v4
	v_cvt_u32_f32_e32 v4, v4
	v_mul_lo_u32 v1, v3, v4
	v_mul_hi_u32 v1, v4, v1
	v_add_u32_e32 v1, v4, v1
	v_mul_hi_u32 v1, v5, v1
	v_mul_lo_u32 v3, v1, v2
	v_sub_u32_e32 v3, v5, v3
	v_add_u32_e32 v4, 1, v1
	v_cmp_ge_u32_e32 vcc, v3, v2
	s_nop 1
	v_cndmask_b32_e32 v1, v1, v4, vcc
	v_sub_u32_e32 v4, v3, v2
	v_cndmask_b32_e32 v3, v3, v4, vcc
	v_add_u32_e32 v4, 1, v1
	v_cmp_ge_u32_e32 vcc, v3, v2
	v_add_u32_e32 v3, 1, v5
	s_nop 0
	v_cndmask_b32_e32 v1, v1, v4, vcc
	v_mul_lo_u32 v4, v2, v1
	v_add_u32_e32 v2, v4, v2
	v_readlane_b32 s100, v235, 7
	v_readlane_b32 s101, v235, 8
	v_add_u32_e32 v236, 1, v1
	s_waitcnt lgkmcnt(0)
	v_mul_lo_u32 v236, v236, v0
	v_mov_b32_e32 v237, 0x3400
	v_mov_b32_e32 v239, 0
	v_cmp_ne_u32_e32 vcc, v3, v2
	s_cbranch_vccnz .Lxb_poll_0
	buffer_wbl2 sc1
	s_waitcnt vmcnt(0)
	v_mov_b32_e32 v238, 1
	global_atomic_add v237, v238, s[100:101]
.Lxb_poll_0:
	global_load_dword v238, v237, s[100:101] sc1
	s_waitcnt vmcnt(0)
	v_cmp_ge_u32_e32 vcc, v238, v236
	s_cbranch_vccnz .Lxb_done_0
	s_sleep 1
	v_add_u32_e32 v239, 1, v239
	v_cmp_gt_u32_e32 vcc, 0x200000, v239
	s_cbranch_vccnz .Lxb_poll_0
.Lxb_done_0:
	s_waitcnt vmcnt(0)
.LBB0_137:
	s_or_b64 exec, exec, s[0:1]
	s_mov_b64 s[12:13], s[46:47]
	v_mov_b32_e32 v148, v186
	s_waitcnt lgkmcnt(0)
	s_barrier
	s_load_dwordx2 s[0:1], s[12:13], 0x98
	v_add_u32_e32 v0, s33, v148
	s_movk_i32 s2, 0x4800
	v_cmp_gt_i32_e32 vcc, s2, v0
	s_and_saveexec_b64 s[2:3], vcc
	s_cbranch_execz .LBB0_140
	s_load_dwordx2 s[4:5], s[12:13], 0x28
	v_ashrrev_i32_e32 v1, 31, v0
	s_ashr_i32 s27, s26, 31
	s_waitcnt lgkmcnt(0)
	v_lshl_add_u64 v[2:3], v[0:1], 2, s[0:1]
	s_lshl_b64 s[6:7], s[26:27], 2
	s_mov_b64 s[8:9], 0
	s_mov_b32 s10, 0x2aaaaaab
	s_movk_i32 s11, 0x47ff

.LBB0_171:
	s_mov_b64 s[4:5], exec
	v_readlane_b32 s2, v235, 9
	s_lshl_b32 s2, s2, 8
	v_readlane_b32 s8, v235, 7
	v_mbcnt_lo_u32_b32 v1, s4, 0
	v_readlane_b32 s9, v235, 8
	s_add_u32 s2, s8, s2
	v_mbcnt_hi_u32_b32 v1, s5, v1
	s_addc_u32 s3, s9, 0
	v_cmp_eq_u32_e32 vcc, 0, v1
	s_and_saveexec_b64 s[8:9], vcc
	s_cbranch_execz .LBB0_173
	s_bcnt1_i32_b64 s4, s[4:5]
	v_mov_b32_e32 v3, 0x1000
	v_mov_b32_e32 v4, s4
	global_atomic_add v3, v3, v4, s[2:3] offset:1024 sc0
	buffer_inv sc1
.LBB0_173:
	s_or_b64 exec, exec, s[8:9]
	v_cvt_f32_u32_e32 v4, v2
	s_waitcnt vmcnt(1)
	v_readfirstlane_b32 s4, v3
	v_sub_u32_e32 v3, 0, v2
	v_rcp_iflag_f32_e32 v4, v4
	v_add_u32_e32 v5, s4, v1
	v_mul_f32_e32 v4, 0x4f7ffffe, v4
	v_cvt_u32_f32_e32 v4, v4
	v_mul_lo_u32 v1, v3, v4
	v_mul_hi_u32 v1, v4, v1
	v_add_u32_e32 v1, v4, v1
	v_mul_hi_u32 v1, v5, v1
	v_mul_lo_u32 v3, v1, v2
	v_sub_u32_e32 v3, v5, v3
	v_add_u32_e32 v4, 1, v1
	v_cmp_ge_u32_e32 vcc, v3, v2
	s_nop 1
	v_cndmask_b32_e32 v1, v1, v4, vcc
	v_sub_u32_e32 v4, v3, v2
	v_cndmask_b32_e32 v3, v3, v4, vcc
	v_add_u32_e32 v4, 1, v1
	v_cmp_ge_u32_e32 vcc, v3, v2
	v_add_u32_e32 v3, 1, v5
	s_nop 0
	v_cndmask_b32_e32 v1, v1, v4, vcc
	v_mul_lo_u32 v4, v2, v1
	v_add_u32_e32 v2, v4, v2
	v_readlane_b32 s100, v235, 7
	v_readlane_b32 s101, v235, 8
	v_add_u32_e32 v236, 1, v1
	s_waitcnt lgkmcnt(0)
	v_mul_lo_u32 v236, v236, v0
	v_mov_b32_e32 v237, 0x3400
	v_mov_b32_e32 v239, 0
	v_cmp_ne_u32_e32 vcc, v3, v2
	s_cbranch_vccnz .Lxb_poll_1
	buffer_wbl2 sc1
	s_waitcnt vmcnt(0)
	v_mov_b32_e32 v238, 1
	global_atomic_add v237, v238, s[100:101]

.Lxb_done_1:
	s_waitcnt vmcnt(0)
.LBB0_208:
	s_or_b64 exec, exec, s[0:1]
	v_readlane_b32 s8, v235, 0
	v_readlane_b32 s10, v235, 2
	s_mul_i32 s0, s10, 33
	s_lshr_b32 s4, s0, 6
	s_cmp_gt_i32 s10, 63
	s_cselect_b64 s[0:1], -1, 0
	s_and_b64 s[2:3], s[0:1], exec
	s_cselect_b32 s27, s4, s10
	s_ashr_i32 s17, s52, 31
	s_lshr_b32 s2, s17, 29
	s_add_i32 s2, s52, s2
	s_ashr_i32 s62, s2, 3
	s_and_b32 s2, s2, -8
	s_sub_i32 s63, s52, s2
	v_readlane_b32 s11, v235, 3
	s_mov_b32 s16, s52
	s_cmp_lt_i32 s63, 0
	v_readlane_b32 s9, v235, 1
	s_cselect_b64 s[4:5], -1, 0
	s_cmp_lt_i32 s52, s27
	s_mov_b64 s[10:11], s[46:47]
	v_writelane_b32 v235, s16, 16
	s_waitcnt lgkmcnt(0)
	s_barrier
	v_writelane_b32 v235, s17, 17
	s_cbranch_scc0 .LBB0_265
	s_cmpk_lt_i32 s16, 0x318
	v_mov_b32_e32 v8, v186
	s_cselect_b64 s[2:3], -1, 0
	s_cmpk_gt_i32 s16, 0x317
	s_nop 0
	v_readfirstlane_b32 s20, v8
	s_cbranch_scc1 .LBB0_211
	s_movk_i32 s12, 0x64
	s_and_b64 s[8:9], s[4:5], exec
	s_cselect_b32 s8, s12, 0x63
	s_mul_i32 s8, s63, s8
	s_add_i32 s8, s8, s62
	s_mul_hi_i32 s9, s8, 0x2aaaaaab
	s_lshr_b32 s12, s9, 31
	s_ashr_i32 s9, s9, 4
	s_add_i32 s9, s9, s12
	s_lshl_b32 s12, s9, 3
	s_sub_i32 s13, 0x42, s12
	s_min_u32 s13, s13, 8
	s_mulk_i32 s9, 0x60
	s_sub_i32 s14, s8, s9
	v_cvt_f32_ubyte0_e32 v1, s13
	v_cvt_f32_i32_e32 v0, s14
	v_rcp_iflag_f32_e32 v2, v1
	s_ashr_i32 s8, s14, 30
	s_or_b32 s15, s8, 1
	v_mul_f32_e32 v2, v0, v2
	v_trunc_f32_e32 v2, v2
	v_fma_f32 v0, -v2, v1, v0
	v_cvt_i32_f32_e32 v2, v2
	v_cmp_ge_f32_e64 s[8:9], |v0|, v1
	s_and_b64 s[8:9], s[8:9], exec
	s_cselect_b32 s8, s15, 0
	v_readfirstlane_b32 s9, v2
	s_add_i32 s9, s9, s8
	s_sext_i32_i8 s8, s9
	s_mul_i32 s9, s9, s13
	s_sub_i32 s9, s14, s9
	s_sext_i32_i8 s9, s9
	s_add_i32 s54, s12, s9

.LBB0_309:
	s_mov_b64 s[8:9], exec
	v_readlane_b32 s2, v235, 9
	s_lshl_b32 s2, s2, 8
	v_readlane_b32 s10, v235, 7
	v_mbcnt_lo_u32_b32 v1, s8, 0
	v_readlane_b32 s11, v235, 8
	s_add_u32 s2, s10, s2
	v_mbcnt_hi_u32_b32 v1, s9, v1
	s_addc_u32 s3, s11, 0
	v_cmp_eq_u32_e32 vcc, 0, v1
	s_and_saveexec_b64 s[10:11], vcc
	s_cbranch_execz .LBB0_311
	s_bcnt1_i32_b64 s8, s[8:9]
	v_mov_b32_e32 v3, 0x1000
	v_mov_b32_e32 v4, s8
	global_atomic_add v3, v3, v4, s[2:3] offset:1024 sc0
	buffer_inv sc1
.LBB0_311:
	s_or_b64 exec, exec, s[10:11]
	v_cvt_f32_u32_e32 v4, v2
	s_waitcnt vmcnt(1)
	v_readfirstlane_b32 s8, v3
	v_sub_u32_e32 v3, 0, v2
	v_rcp_iflag_f32_e32 v4, v4
	v_add_u32_e32 v5, s8, v1
	v_mul_f32_e32 v4, 0x4f7ffffe, v4
	v_cvt_u32_f32_e32 v4, v4
	v_mul_lo_u32 v1, v3, v4
	v_mul_hi_u32 v1, v4, v1
	v_add_u32_e32 v1, v4, v1
	v_mul_hi_u32 v1, v5, v1
	v_mul_lo_u32 v3, v1, v2
	v_sub_u32_e32 v3, v5, v3
	v_add_u32_e32 v4, 1, v1
	v_cmp_ge_u32_e32 vcc, v3, v2
	s_nop 1
	v_cndmask_b32_e32 v1, v1, v4, vcc
	v_sub_u32_e32 v4, v3, v2
	v_cndmask_b32_e32 v3, v3, v4, vcc
	v_add_u32_e32 v4, 1, v1
	v_cmp_ge_u32_e32 vcc, v3, v2
	v_add_u32_e32 v3, 1, v5
	s_nop 0
	v_cndmask_b32_e32 v1, v1, v4, vcc
	v_mul_lo_u32 v4, v2, v1
	v_add_u32_e32 v2, v4, v2
	v_readlane_b32 s100, v235, 7
	v_readlane_b32 s101, v235, 8
	v_add_u32_e32 v236, 1, v1
	s_waitcnt lgkmcnt(0)
	v_mul_lo_u32 v236, v236, v0
	v_mov_b32_e32 v237, 0x3400
	v_mov_b32_e32 v239, 0
	v_cmp_ne_u32_e32 vcc, v3, v2
	s_cbranch_vccnz .Lxb_poll_2
	buffer_wbl2 sc1
	s_waitcnt vmcnt(0)
	v_mov_b32_e32 v238, 1
	global_atomic_add v237, v238, s[100:101]

.Lxb_done_2:
	s_waitcnt vmcnt(0)
.LBB0_346:
	s_or_b64 exec, exec, s[0:1]
	s_mov_b64 s[0:1], s[46:47]
	v_mov_b32_e32 v66, v186
	s_waitcnt lgkmcnt(0)
	s_barrier
	s_load_dwordx2 s[2:3], s[0:1], 0x98
	v_readlane_b32 s0, v235, 16
	s_cmpk_lt_i32 s0, 0x140
	v_readlane_b32 s1, v235, 17
	s_cbranch_scc0 .LBB0_368
	s_waitcnt lgkmcnt(0)
	s_add_u32 s28, s2, 0x176f3000
	s_addc_u32 s29, s3, 0
	s_add_u32 s27, s2, 0xf1f3000
	v_and_b32_e32 v0, 63, v66
	s_addc_u32 s40, s3, 0
	s_add_u32 s30, s2, 0xd0f3000
	v_lshlrev_b32_e32 v40, 2, v0
	v_mov_b32_e32 v41, 0
	s_addc_u32 s31, s3, 0
	v_lshl_add_u64 v[0:1], s[2:3], 0, v[40:41]
	s_mov_b64 s[0:1], 0x152f3000
	s_add_u32 s34, s2, 0xc073000
	v_lshl_add_u64 v[42:43], v[0:1], 0, s[0:1]
	s_movk_i32 s41, 0x80
	v_readlane_b32 s0, v235, 16
	v_ashrrev_i32_e32 v67, 6, v66
	s_addc_u32 s35, s3, 0
	v_cmp_gt_i32_e64 s[8:9], s41, v66
	s_movk_i32 s42, 0x90
	s_mov_b32 s37, 0
	s_add_i32 s43, 0, 0x1d200
	s_mov_b32 s44, 0x1771b000
	s_add_i32 s45, 0, 0x18a00
	s_add_i32 s46, 0, 0x14200
	s_movk_i32 s47, 0x110
	s_mov_b32 s48, 0x5040100
	s_add_i32 s49, 0, 0x9800
	s_movk_i32 s50, 0x1000
	v_mov_b32_e32 v130, v41
	v_mov_b32_e32 v131, v41
	s_mov_b32 s51, s0
	v_readlane_b32 s1, v235, 17
	s_branch .LBB0_349

.Lxb_done_3:
	s_waitcnt vmcnt(0)
.LBB0_426:
	s_or_b64 exec, exec, s[0:1]
	s_mov_b64 s[0:1], s[46:47]
	s_waitcnt lgkmcnt(0)
	s_barrier
	v_mov_b32_e32 v0, v186
	s_load_dwordx2 s[0:1], s[0:1], 0x98
	v_add_u32_e32 v2, s33, v0
	s_mov_b32 s2, 0x20000
	v_cmp_gt_i32_e32 vcc, s2, v2
	s_and_saveexec_b64 s[2:3], vcc
	s_cbranch_execz .LBB0_429
	s_waitcnt lgkmcnt(0)
	s_add_u32 s8, s0, 0x152f3000
	s_addc_u32 s9, s1, 0
	s_add_u32 s10, s0, 0x176f3000
	s_addc_u32 s11, s1, 0
	v_readlane_b32 s14, v235, 16
	v_readlane_b32 s16, v235, 0
	s_add_u32 s12, s0, 0x166f3000
	v_lshlrev_b32_e32 v0, 1, v0
	v_readlane_b32 s15, v235, 17
	v_readlane_b32 s17, v235, 1
	v_readlane_b32 s18, v235, 2
	s_addc_u32 s13, s1, 0
	v_lshl_add_u32 v3, s14, 10, v0
	s_lshl_b32 s16, s18, 10
	s_mov_b64 s[14:15], 0
	v_mov_b32_e32 v1, 0
	s_mov_b32 s17, 0x1ffff
	v_readlane_b32 s19, v235, 3

.Lxb_done_4:
	s_waitcnt vmcnt(0)
.LBB0_491:
	s_or_b64 exec, exec, s[0:1]
	v_readlane_b32 s0, v235, 16
	v_readlane_b32 s1, v235, 17
	s_lshl_b32 s8, s0, 4
	v_readlane_b32 s0, v235, 0
	v_readlane_b32 s1, v235, 1
	s_mov_b64 s[14:15], s[46:47]
	s_waitcnt lgkmcnt(0)
	v_mov_b32_e32 v0, v186
	s_barrier
	s_load_dwordx2 s[0:1], s[14:15], 0x98
	s_waitcnt vmcnt(14)
	v_ashrrev_i32_e32 v68, 5, v0
	v_readlane_b32 s2, v235, 2
	v_and_b32_e32 v1, -2, v68
	s_lshl_b32 s20, s2, 4
	v_add_u32_e32 v70, s8, v1
	s_movk_i32 s2, 0x2000
	v_readlane_b32 s3, v235, 3
	v_cmp_gt_i32_e32 vcc, s2, v70
	v_writelane_b32 v235, s8, 18
	s_and_saveexec_b64 s[2:3], vcc
	s_cbranch_execz .LBB0_494
	v_bfe_u32 v69, v0, 4, 2
	v_and_b32_e32 v71, 15, v0
	v_lshlrev_b32_e32 v64, 4, v69
	v_mov_b32_e32 v65, 0
	v_lshlrev_b32_e32 v0, 8, v71
	v_mov_b32_e32 v1, v65
	s_waitcnt lgkmcnt(0)
	v_lshl_add_u64 v[66:67], s[0:1], 0, v[64:65]
	v_lshl_add_u64 v[48:49], v[66:67], 0, v[0:1]
	v_add_co_u32_e32 v18, vcc, 0x1adb000, v48
	s_mov_b64 s[8:9], 0x1adb000
	s_nop 0
	v_addc_co_u32_e32 v19, vcc, 0, v49, vcc
	v_add_co_u32_e32 v32, vcc, 0x1adc000, v48
	v_lshl_add_u64 v[16:17], v[48:49], 0, s[8:9]
	s_nop 0
	v_addc_co_u32_e32 v33, vcc, 0, v49, vcc
	v_add_co_u32_e32 v50, vcc, 0x1add000, v48
	global_load_dwordx4 v[0:3], v[16:17], off offset:64
	global_load_dwordx4 v[4:7], v[16:17], off offset:128
	global_load_dwordx4 v[8:11], v[18:19], off
	global_load_dwordx4 v[12:15], v[16:17], off offset:192
	v_addc_co_u32_e32 v51, vcc, 0, v49, vcc
	s_waitcnt vmcnt(17)
	v_add_co_u32_e32 v72, vcc, 0x1ade000, v48
	global_load_dwordx4 v[16:19], v[32:33], off
	global_load_dwordx4 v[20:23], v[32:33], off offset:64
	global_load_dwordx4 v[24:27], v[32:33], off offset:128
	global_load_dwordx4 v[28:31], v[32:33], off offset:192
	v_addc_co_u32_e32 v73, vcc, 0, v49, vcc
	global_load_dwordx4 v[32:35], v[50:51], off
	global_load_dwordx4 v[36:39], v[50:51], off offset:64
	global_load_dwordx4 v[40:43], v[50:51], off offset:128
	global_load_dwordx4 v[44:47], v[50:51], off offset:192
	s_nop 0
	global_load_dwordx4 v[48:51], v[72:73], off
	global_load_dwordx4 v[52:55], v[72:73], off offset:64
	global_load_dwordx4 v[56:59], v[72:73], off offset:128
	global_load_dwordx4 v[60:63], v[72:73], off offset:192
	s_mov_b64 s[10:11], 0x132f3000
	v_lshl_add_u64 v[66:67], v[66:67], 0, s[10:11]
	v_lshrrev_b32_e32 v64, 1, v68
	v_readlane_b32 s10, v235, 16
	v_readlane_b32 s16, v235, 0
	s_add_u32 s8, s0, 0x1971b000
	v_lshlrev_b32_e32 v68, 2, v64
	v_readlane_b32 s11, v235, 17
	v_readlane_b32 s17, v235, 1
	v_readlane_b32 s18, v235, 2
	v_lshlrev_b32_e32 v64, 5, v64
	s_addc_u32 s9, s1, 0
	v_lshlrev_b32_e32 v72, 9, v69
	v_lshl_add_u32 v73, s10, 5, v68
	s_lshl_b32 s12, s18, 5
	v_lshl_add_u32 v74, s10, 8, v64
	s_lshl_b32 s13, s18, 8
	s_mov_b64 s[10:11], 0
	s_movk_i32 s16, 0x60
	s_movk_i32 s17, 0x1fff
	v_readlane_b32 s19, v235, 3

.LBB0_516:
	s_mov_b64 s[6:7], exec
	v_readlane_b32 s2, v235, 9
	s_lshl_b32 s2, s2, 8
	v_readlane_b32 s8, v235, 7
	v_mbcnt_lo_u32_b32 v1, s6, 0
	v_readlane_b32 s9, v235, 8
	s_add_u32 s2, s8, s2
	v_mbcnt_hi_u32_b32 v1, s7, v1
	s_addc_u32 s3, s9, 0
	v_cmp_eq_u32_e32 vcc, 0, v1
	s_and_saveexec_b64 s[8:9], vcc
	s_cbranch_execz .LBB0_518
	s_bcnt1_i32_b64 s6, s[6:7]
	v_mov_b32_e32 v3, 0x1000
	v_mov_b32_e32 v4, s6
	global_atomic_add v3, v3, v4, s[2:3] offset:1024 sc0
	buffer_inv sc1
.LBB0_518:
	s_or_b64 exec, exec, s[8:9]
	v_cvt_f32_u32_e32 v4, v2
	s_waitcnt vmcnt(1)
	v_readfirstlane_b32 s6, v3
	v_sub_u32_e32 v3, 0, v2
	v_rcp_iflag_f32_e32 v4, v4
	v_add_u32_e32 v5, s6, v1
	v_mul_f32_e32 v4, 0x4f7ffffe, v4
	v_cvt_u32_f32_e32 v4, v4
	v_mul_lo_u32 v1, v3, v4
	v_mul_hi_u32 v1, v4, v1
	v_add_u32_e32 v1, v4, v1
	v_mul_hi_u32 v1, v5, v1
	v_mul_lo_u32 v3, v1, v2
	v_sub_u32_e32 v3, v5, v3
	v_add_u32_e32 v4, 1, v1
	v_cmp_ge_u32_e32 vcc, v3, v2
	s_nop 1
	v_cndmask_b32_e32 v1, v1, v4, vcc
	v_sub_u32_e32 v4, v3, v2
	v_cndmask_b32_e32 v3, v3, v4, vcc
	v_add_u32_e32 v4, 1, v1
	v_cmp_ge_u32_e32 vcc, v3, v2
	v_add_u32_e32 v3, 1, v5
	s_nop 0
	v_cndmask_b32_e32 v1, v1, v4, vcc
	v_mul_lo_u32 v4, v2, v1
	v_add_u32_e32 v2, v4, v2
	v_readlane_b32 s100, v235, 7
	v_readlane_b32 s101, v235, 8
	v_add_u32_e32 v236, 1, v1
	s_waitcnt lgkmcnt(0)
	v_mul_lo_u32 v236, v236, v0
	v_mov_b32_e32 v237, 0x3400
	v_mov_b32_e32 v239, 0
	v_cmp_ne_u32_e32 vcc, v3, v2
	s_cbranch_vccnz .Lxb_poll_5
	buffer_wbl2 sc1
	s_waitcnt vmcnt(0)
	v_mov_b32_e32 v238, 1
	global_atomic_add v237, v238, s[100:101]

.Lxb_done_5:
	s_waitcnt vmcnt(0)
.LBB0_553:
	s_or_b64 exec, exec, s[0:1]
	s_mov_b64 s[6:7], s[46:47]
	v_mov_b32_e32 v8, v186
	s_waitcnt lgkmcnt(0)
	s_barrier
	s_and_b64 vcc, exec, s[24:25]
	v_readfirstlane_b32 s11, v8
	s_cbranch_vccz .LBB0_573
	v_lshlrev_b32_e32 v0, 4, v8
	v_add_u32_e32 v1, 0x2000, v0
	v_ashrrev_i32_e32 v2, 31, v1
	v_lshrrev_b32_e32 v2, 22, v2
	v_add_u32_e32 v2, v1, v2
	v_ashrrev_i32_e32 v9, 10, v2
	v_mul_i32_i24_e32 v3, 0x400, v9
	v_sub_u32_e32 v1, v1, v3
	v_lshrrev_b32_e32 v3, 4, v1
	v_bitop3_b32 v1, v3, v1, 32 bitop3:0x6c
	v_ashrrev_i32_e32 v3, 31, v1
	v_lshrrev_b32_e32 v3, 26, v3
	v_add_u32_e32 v3, v1, v3
	v_ashrrev_i32_e32 v10, 6, v3
	v_and_b32_e32 v3, 0xc0, v3
	v_sub_u32_e32 v1, v1, v3
	v_mov_b32_e32 v3, 1
	v_lshlrev_b32_e32 v2, 5, v9
	v_ashrrev_i16_sdwa v1, v3, sext(v1) dst_sel:DWORD dst_unused:UNUSED_PAD src0_sel:DWORD src1_sel:BYTE_0
	v_and_b32_e32 v2, 32, v2
	v_bfe_i32 v11, v1, 0, 16
	v_add_lshl_u32 v1, v2, v11, 1
	v_lshlrev_b32_e32 v2, 3, v9
	v_and_b32_e32 v2, -16, v2
	s_load_dwordx2 s[0:1], s[6:7], 0x98
	s_load_dwordx2 s[2:3], s[6:7], 0x0
	v_add_u32_e32 v2, v10, v2
	v_and_b32_e32 v4, 3, v10
	s_mov_b32 s6, 0x1fffe0
	v_lshl_add_u32 v136, v2, 11, v1
	v_and_or_b32 v4, v2, s6, v4
	v_lshrrev_b32_e32 v5, 2, v2
	v_lshlrev_b32_e32 v2, 1, v2
	v_and_b32_e32 v5, 4, v5
	v_and_b32_e32 v2, 24, v2
	v_or3_b32 v2, v4, v5, v2
	v_lshl_add_u32 v140, v2, 11, v1
	v_bfe_i32 v2, v8, 27, 1
	v_lshrrev_b32_e32 v2, 22, v2
	v_add_u32_e32 v2, v0, v2
	v_and_b32_e32 v2, 0xfffffc00, v2
	v_sub_u32_e32 v0, v0, v2
	v_lshrrev_b32_e32 v2, 4, v0
	v_bitop3_b32 v2, v2, v0, 32 bitop3:0x6c
	v_ashrrev_i32_e32 v0, 31, v0
	v_lshrrev_b32_e32 v0, 26, v0
	v_ashrrev_i32_e32 v1, 31, v8
	v_add_u32_e32 v0, v2, v0
	v_lshrrev_b32_e32 v1, 26, v1
	v_ashrrev_i32_e32 v13, 6, v0
	v_add_u32_e32 v1, v8, v1
	v_mul_i32_i24_e32 v0, 64, v13
	v_ashrrev_i32_e32 v12, 6, v1
	v_sub_u32_e32 v0, v2, v0
	s_waitcnt lgkmcnt(0)
	s_add_u32 s33, s0, 0x1971b000
	v_lshlrev_b32_e32 v1, 5, v12
	v_ashrrev_i16_sdwa v0, v3, sext(v0) dst_sel:DWORD dst_unused:UNUSED_PAD src0_sel:DWORD src1_sel:BYTE_0
	s_addc_u32 s42, s1, 0
	v_and_b32_e32 v1, 32, v1
	v_bfe_i32 v14, v0, 0, 16
	s_add_u32 s43, s0, 0x87b000
	v_add_lshl_u32 v0, v1, v14, 1
	v_lshlrev_b32_e32 v1, 3, v12
	s_addc_u32 s44, s1, 0
	s_ashr_i32 s8, s11, 6
	v_and_b32_e32 v1, -16, v1
	s_ashr_i32 s12, s11, 8
	s_lshl_b32 s45, s8, 10
	v_add_u32_e32 v1, v13, v1
	v_and_b32_e32 v2, 3, v13
	s_lshl_b32 s7, s63, 5
	v_and_or_b32 v2, v1, s6, v2
	s_mul_i32 s6, s63, 33
	s_and_b64 s[4:5], s[4:5], exec
	s_cselect_b32 s4, s6, s7
	s_add_i32 s4, s4, s62
	s_ashr_i32 s5, s4, 31
	s_lshr_b32 s5, s5, 27
	s_add_i32 s5, s4, s5
	s_ashr_i32 s6, s5, 5
	s_and_b32 s5, s5, 0xffe0
	s_sub_i32 s4, s4, s5
	s_bfe_i32 s5, s4, 0x80000
	s_bfe_u32 s5, s5, 0x3000c
	s_add_i32 s5, s4, s5
	s_bfe_i32 s7, s5, 0x80000
	s_and_b32 s5, s5, 0xf8
	s_sub_i32 s4, s4, s5
	s_lshl_b32 s6, s6, 3
	s_sext_i32_i16 s7, s7
	s_sext_i32_i8 s4, s4
	s_lshr_b32 s10, s7, 3
	s_add_i32 s34, s6, s4
	s_ashr_i32 s35, s34, 31
	s_bfe_i64 s[6:7], s[10:11], 0x100000
	v_lshl_add_u32 v142, v1, 11, v0
	v_lshrrev_b32_e32 v3, 2, v1
	v_lshlrev_b32_e32 v1, 1, v1
	s_lshl_b64 s[4:5], s[34:35], 19
	s_lshl_b64 s[6:7], s[6:7], 19
	v_and_b32_e32 v3, 4, v3
	v_and_b32_e32 v1, 24, v1
	s_add_u32 s38, s43, s6
	v_or3_b32 v1, v2, v3, v1
	s_addc_u32 s39, s44, s7
	s_add_i32 s46, s45, 0
	v_lshl_add_u32 v146, v1, 11, v0
	s_add_i32 m0, s46, 0x10000
	v_add_u32_e32 v144, 0x40000, v142
	global_load_lds_dwordx4 v146, s[38:39]
	s_add_i32 m0, s46, 0x12000
	s_add_u32 s6, s38, 0x40000
	global_load_lds_dwordx4 v140, s[38:39]
	s_addc_u32 s7, s39, 0
	s_add_i32 m0, s46, 0x14000
	v_add_u32_e32 v138, 0x40000, v136
	global_load_lds_dwordx4 v146, s[6:7]
	s_add_i32 m0, s46, 0x16000
	s_add_u32 s36, s33, s4
	global_load_lds_dwordx4 v140, s[6:7]
	s_addc_u32 s37, s42, s5
	s_mov_b32 m0, s46
	s_add_i32 s47, s46, 0x2000
	global_load_lds_dwordx4 v142, s[36:37]
	s_mov_b32 m0, s47
	s_add_i32 s48, s46, 0x4000
	global_load_lds_dwordx4 v136, s[36:37]
	s_mov_b32 m0, s48
	s_add_i32 s49, s46, 0x6000
	global_load_lds_dwordx4 v144, s[36:37]
	s_mov_b32 m0, s49
	v_mov_b32_e32 v147, 0
	global_load_lds_dwordx4 v138, s[36:37]
	v_mov_b32_e32 v141, v147
	v_mov_b32_e32 v143, v147
	v_mov_b32_e32 v137, v147
	s_cmp_eq_u32 s12, 1
	s_mov_b32 s13, 0x40000
	s_mov_b32 s50, 0
	v_lshl_add_u64 v[6:7], s[38:39], 0, v[146:147]
	v_lshl_add_u64 v[4:5], s[38:39], 0, v[140:141]
	v_lshl_add_u64 v[0:1], s[36:37], 0, v[142:143]
	s_cselect_b64 s[4:5], -1, 0
	s_cmp_lg_u32 s12, 1
	v_lshl_add_u64 v[2:3], s[36:37], 0, v[136:137]
	s_cbranch_scc1 .LBB0_556
	s_barrier

.Lxb_done_6:
	s_waitcnt vmcnt(0)
.LBB0_626:
	s_or_b64 exec, exec, s[0:1]
	s_mov_b64 s[22:23], s[46:47]
	v_mov_b32_e32 v32, v186
	s_and_b64 vcc, exec, s[24:25]
	s_waitcnt lgkmcnt(0)
	s_barrier
	s_cbranch_vccz .LBB0_659
	s_load_dwordx2 s[24:25], s[22:23], 0x98
	s_load_dwordx2 s[26:27], s[22:23], 0x68
	v_and_b32_e32 v3, 63, v32
	v_mov_b32_e32 v35, 0
	v_lshlrev_b32_e32 v0, 3, v3
	s_waitcnt lgkmcnt(0)
	s_add_u32 s28, s24, 0x1b000
	s_addc_u32 s29, s25, 0
	s_add_u32 s0, s24, 0x9f73000
	s_addc_u32 s1, s25, 0
	v_mov_b32_e32 v1, v35
	v_lshl_add_u64 v[36:37], s[0:1], 0, v[0:1]
	v_mbcnt_hi_u32_b32 v0, -1, v187
	v_and_b32_e32 v1, 64, v0
	v_add_u32_e32 v1, 64, v1
	v_xor_b32_e32 v7, 32, v0
	v_cmp_lt_i32_e32 vcc, v7, v1
	v_ashrrev_i32_e32 v2, 6, v32
	v_and_b32_e32 v8, 1, v2
	v_cndmask_b32_e32 v7, v0, v7, vcc
	v_lshlrev_b32_e32 v104, 2, v7
	v_xor_b32_e32 v7, 16, v0
	v_cmp_lt_i32_e32 vcc, v7, v1
	v_bfe_u32 v9, v32, 4, 2
	v_lshlrev_b32_e32 v34, 2, v3
	v_cndmask_b32_e32 v7, v0, v7, vcc
	v_lshlrev_b32_e32 v105, 2, v7
	v_xor_b32_e32 v7, 8, v0
	v_cmp_lt_i32_e32 vcc, v7, v1
	v_lshlrev_b32_e32 v6, 4, v3
	v_lshlrev_b32_e32 v103, 3, v2
	v_cndmask_b32_e32 v7, v0, v7, vcc
	v_lshlrev_b32_e32 v106, 2, v7
	v_xor_b32_e32 v7, 4, v0
	v_cmp_lt_i32_e32 vcc, v7, v1
	v_cmp_eq_u32_e64 s[10:11], 0, v3
	v_mov_b32_e32 v3, v35
	v_cndmask_b32_e32 v7, v0, v7, vcc
	v_lshlrev_b32_e32 v107, 2, v7
	v_xor_b32_e32 v7, 2, v0
	v_cmp_lt_i32_e32 vcc, v7, v1
	v_and_b32_e32 v111, 15, v32
	s_movk_i32 s44, 0x2040
	v_cndmask_b32_e32 v7, v0, v7, vcc
	v_lshlrev_b32_e32 v108, 2, v7
	v_xor_b32_e32 v7, 1, v0
	v_cmp_lt_i32_e32 vcc, v7, v1
	v_mov_b32_e32 v1, v35
	v_ashrrev_i32_e32 v41, 4, v32
	v_cndmask_b32_e32 v0, v0, v7, vcc
	v_lshlrev_b32_e32 v109, 2, v0
	v_lshl_add_u32 v0, v2, 5, 0
	v_add_u32_e32 v110, 0x10240, v0
	v_lshlrev_b32_e32 v0, 10, v8
	v_lshl_add_u64 v[0:1], s[0:1], 0, v[0:1]
	v_lshlrev_b32_e32 v2, 8, v9
	v_lshl_add_u64 v[38:39], v[0:1], 0, v[2:3]
	v_lshl_or_b32 v0, v8, 2, v9
	v_ashrrev_i32_e32 v7, 7, v32
	v_mad_u32_u24 v2, v0, s44, 0
	v_lshl_add_u32 v0, v111, 2, 0
	v_lshlrev_b32_e32 v45, 2, v32
	s_add_i32 s0, 0, 0x10340
	v_add_u32_e32 v113, 0x10200, v0
	v_lshl_add_u32 v0, v7, 6, 0
	v_and_b32_e32 v4, 60, v45
	v_and_b32_e32 v5, 3, v41
	v_lshlrev_b32_e32 v112, 4, v7
	v_cmp_eq_u32_e64 s[12:13], 0, v8
	v_cmp_eq_u32_e64 s[14:15], 1, v8
	v_lshl_add_u32 v8, v7, 10, s0
	v_add_u32_e32 v7, 0x10240, v0
	v_and_b32_e32 v0, 0x7c0, v32
	v_lshl_add_u32 v0, v0, 2, 0
	v_lshlrev_b32_e32 v116, 2, v4
	v_lshlrev_b32_e32 v117, 2, v5
	v_add3_u32 v40, v0, v116, v117
	v_max_i32_e32 v0, 0x200, v32
	v_sub_u32_e32 v0, v0, v32
	v_add_u32_e32 v0, 0x1ff, v0
	s_movk_i32 s2, 0x400
	v_add_u32_e32 v98, 0, v45
	v_lshrrev_b32_e32 v1, 9, v0
	v_cmp_gt_i32_e64 s[6:7], s2, v32
	s_add_i32 s2, 0, 0x11340
	v_lshlrev_b32_e32 v114, 2, v9
	v_add_u32_e32 v118, 0x11340, v98
	v_add_u32_e32 v4, 0x12340, v98
	v_add_u32_e32 v5, 1, v1
	v_add_u32_e32 v9, -1, v1
	s_movk_i32 s0, 0x35ff
	v_lshlrev_b32_e32 v1, 11, v1
	v_add_u32_e32 v101, s2, v6
	v_cmp_lt_u32_e32 vcc, s0, v0
	v_add_u32_e32 v12, v118, v1
	v_cmp_gt_u32_e64 s[2:3], 2.0, v0
	v_add_u32_e32 v0, v4, v1
	v_cmp_lt_u32_e64 s[0:1], v12, v118
	v_cmp_lt_u32_e64 s[4:5], v0, v4
	s_or_b64 s[0:1], s[4:5], s[0:1]
	s_xor_b64 s[0:1], s[0:1], -1
	v_lshrrev_b32_e32 v11, 1, v9
	s_and_b64 s[0:1], s[0:1], s[2:3]
	v_and_b32_e32 v0, 0xfffffe, v5
	v_add_u32_e32 v11, 1, v11
	v_lshl_add_u32 v119, v0, 9, v32
	v_cmp_ne_u32_e64 s[20:21], v5, v0
	s_and_b64 s[2:3], vcc, s[0:1]
	v_lshl_add_u64 v[0:1], s[24:25], 0, v[34:35]
	s_mov_b64 s[0:1], 0xe173000
	v_readlane_b32 s36, v235, 0
	s_add_i32 s31, 0, 0x12340
	v_lshlrev_b32_e32 v3, 4, v111
	v_and_b32_e32 v10, 48, v32
	v_and_b32_e32 v4, 3, v11
	v_lshl_add_u64 v[42:43], v[0:1], 0, s[0:1]
	v_readlane_b32 s0, v235, 16
	v_readlane_b32 s38, v235, 2
	v_add_u32_e32 v99, 0x10340, v98
	v_cmp_gt_i32_e64 s[8:9], 16, v32
	v_add_u32_e32 v100, 0x10200, v98
	v_add_u32_e32 v102, s31, v6
	v_bfe_u32 v115, v41, 7, 2
	s_movk_i32 s45, 0x1ff
	v_add_u32_e32 v33, 0x200, v32
	v_cmp_lt_u32_e64 s[16:17], 5, v9
	v_and_b32_e32 v120, -4, v11
	v_cmp_ne_u32_e64 s[18:19], 0, v4
	v_lshlrev_b32_e32 v121, 12, v4
	v_lshl_add_u32 v122, s0, 6, v103
	s_lshl_b32 s5, s38, 6
	s_movk_i32 s46, 0x4000
	s_movk_i32 s47, 0x3000
	s_mov_b32 s48, 0x3fffffc
	s_mov_b32 s4, 0x3a800000
	s_mov_b32 s49, 0x800000
	s_mov_b32 s30, 0x45800000
	s_mov_b32 s50, 0xc3e00000
	v_add_u32_e32 v123, v2, v3
	v_add_u32_e32 v124, v7, v10
	s_mov_b32 s51, 0x3fb8aa3b
	s_mov_b32 s53, 0xc2ce8ed0
	s_mov_b32 s54, 0x42b17218
	s_movk_i32 s55, 0x1ff0
	v_mov_b32_e32 v44, 0x358637bd
	v_mov_b32_e32 v125, 0x43e00000
	v_add_u32_e32 v126, v8, v6
	v_mov_b32_e32 v127, 0x7f800000
	s_mov_b32 s56, s0
	v_readlane_b32 s1, v235, 17
	v_readlane_b32 s37, v235, 1
	v_readlane_b32 s39, v235, 3
	s_branch .LBB0_629

.Lxb_done_7:
	s_waitcnt vmcnt(0)
.LBB0_712:
	s_or_b64 exec, exec, s[0:1]
	v_readlane_b32 s0, v235, 0
	v_readlane_b32 s2, v235, 2
	v_readlane_b32 s3, v235, 3
	v_readlane_b32 s1, v235, 1
	s_cmp_gt_i32 s2, 63
	v_readlane_b32 s2, v235, 16
	s_cselect_b64 s[0:1], -1, 0
	s_cmp_lt_i32 s2, 32
	v_readlane_b32 s3, v235, 17
	s_cselect_b64 s[4:5], -1, 0
	s_cmp_gt_i32 s2, 31
	s_cselect_b64 s[2:3], -1, 0
	s_and_b64 s[2:3], s[2:3], s[0:1]
	s_mov_b64 s[6:7], s[46:47]
	s_mov_b64 s[0:1], -1
	s_and_b64 vcc, exec, s[2:3]
	v_readlane_b32 s46, v235, 10
	s_waitcnt lgkmcnt(0)
	s_barrier
	v_readlane_b32 s47, v235, 11
	s_cbranch_vccz .LBB0_724
	v_readlane_b32 s0, v235, 12
	v_readlane_b32 s1, v235, 13
	v_mov_b32_e32 v0, v186
	s_add_i32 s0, s52, s0
	v_readfirstlane_b32 s1, v0
	s_ashr_i32 s12, s1, 6
	s_add_i32 s0, s0, s12
	s_add_i32 s30, s0, 0x8600
	s_cmp_gt_i32 s30, 0x83ff
	s_cbranch_scc1 .LBB0_723
	s_load_dwordx4 s[0:3], s[6:7], 0x70
	s_load_dwordx2 s[8:9], s[6:7], 0x80
	s_load_dwordx2 s[10:11], s[6:7], 0x98
	s_mulk_i32 s12, 0x2100
	v_bfe_u32 v12, v0, 1, 5
	v_lshlrev_b32_e32 v1, 2, v0
	v_bfe_u32 v14, v0, 3, 3
	v_and_b32_e32 v0, 7, v0
	s_add_i32 s12, s12, 0
	v_and_b32_e32 v2, 28, v1
	v_mul_u32_u24_e32 v1, 0x220, v0
	v_lshlrev_b32_e32 v3, 2, v14
	v_lshlrev_b32_e32 v8, 4, v0
	v_add3_u32 v15, s12, v1, v3
	v_add_u32_e32 v0, s12, v8
	v_mul_u32_u24_e32 v1, 0x88, v14
	v_mov_b32_e32 v9, 0
	v_add_u32_e32 v20, v0, v1
	s_add_i32 s31, s46, 0xffffff00
	s_mov_b32 s13, 0
	v_and_b32_e32 v13, 28, v12
	v_or_b32_e32 v16, 8, v14
	v_or_b32_e32 v17, 16, v14
	v_or_b32_e32 v18, 24, v14
	v_lshlrev_b32_e32 v10, 2, v2
	v_mov_b32_e32 v11, v9
	s_mov_b32 s33, 0xc3e00000
	v_mov_b32_e32 v19, 0x43e00000
	v_add_u32_e32 v21, 0x880, v20
	v_add_u32_e32 v22, 0xcc0, v20
	s_branch .LBB0_717

.Lxb_done_8:
	s_waitcnt vmcnt(0)
.LBB0_972:
	s_or_b64 exec, exec, s[0:1]
	v_readlane_b32 s0, v235, 0
	v_readlane_b32 s2, v235, 2
	s_abs_i32 s0, s2
	s_waitcnt lgkmcnt(0)
	v_cvt_f32_u32_e32 v0, s0
	v_readlane_b32 s3, v235, 3
	s_sub_i32 s3, 0, s0
	v_readlane_b32 s1, v235, 1
	v_rcp_iflag_f32_e32 v0, v0
	s_add_i32 s1, s2, 0xaff
	s_xor_b32 s2, s1, s2
	s_abs_i32 s1, s1
	v_mul_f32_e32 v0, 0x4f7ffffe, v0
	v_cvt_u32_f32_e32 v0, v0
	s_ashr_i32 s2, s2, 31
	s_barrier
	v_readfirstlane_b32 s4, v0
	s_mul_i32 s3, s3, s4
	s_mul_hi_u32 s3, s4, s3
	s_add_i32 s4, s4, s3
	s_mul_hi_u32 s3, s1, s4
	s_mul_i32 s4, s3, s0
	s_sub_i32 s1, s1, s4
	s_add_i32 s5, s3, 1
	s_sub_i32 s4, s1, s0
	s_cmp_ge_u32 s1, s0
	s_cselect_b32 s3, s5, s3
	s_cselect_b32 s1, s4, s1
	s_add_i32 s4, s3, 1
	s_cmp_ge_u32 s1, s0
	s_cselect_b32 s0, s4, s3
	s_xor_b32 s0, s0, s2
	s_sub_i32 s2, s0, s2
	s_cmp_gt_i32 s2, 24
	s_cselect_b64 s[0:1], -1, 0
	s_cmp_lt_i32 s2, 25
	s_cbranch_scc1 .LBB0_1030
	v_readlane_b32 s4, v235, 14
	v_readlane_b32 s5, v235, 15
	v_mov_b32_e32 v0, v186
	v_readlane_b32 s10, v235, 12
	v_ashrrev_i32_e32 v2, 6, v0
	s_mov_b32 s2, 0x8000
	v_add_u32_e32 v4, s10, v2
	v_cmp_gt_i32_e32 vcc, s2, v4
	v_readlane_b32 s11, v235, 13
	s_and_saveexec_b64 s[2:3], vcc
	s_cbranch_execz .LBB0_976
	s_load_dwordx2 s[6:7], s[4:5], 0x98
	v_ashrrev_i32_e32 v3, 31, v2
	v_lshlrev_b32_e32 v0, 4, v0
	v_and_b32_e32 v6, 0x3f0, v0
	v_mov_b32_e32 v7, 0
	s_waitcnt lgkmcnt(0)
	s_add_u32 s4, s6, 0x11b000
	s_addc_u32 s5, s7, 0
	s_ashr_i32 s11, s10, 31
	v_lshl_add_u64 v[2:3], v[2:3], 0, s[10:11]
	v_lshlrev_b64 v[2:3], 10, v[2:3]
	v_or_b32_e32 v2, v2, v6
	v_lshl_add_u64 v[0:1], s[6:7], 0, v[6:7]
	s_mov_b64 s[8:9], 0xe173000
	v_lshl_add_u64 v[2:3], s[6:7], 0, v[2:3]
	s_mov_b64 s[6:7], 0xf173000
	s_ashr_i32 s47, s46, 31
	v_lshl_add_u64 v[0:1], v[0:1], 0, s[8:9]
	v_lshl_add_u64 v[2:3], v[2:3], 0, s[6:7]
	s_lshl_b64 s[6:7], s[46:47], 10
	s_mov_b64 s[8:9], 0
	s_movk_i32 s10, 0x3ff
	s_movk_i32 s11, 0x7fff

.LBB0_992:
	s_mov_b64 s[6:7], exec
	v_readlane_b32 s4, v235, 9
	s_lshl_b32 s4, s4, 8
	v_readlane_b32 s8, v235, 7
	v_mbcnt_lo_u32_b32 v1, s6, 0
	v_readlane_b32 s9, v235, 8
	s_add_u32 s4, s8, s4
	v_mbcnt_hi_u32_b32 v1, s7, v1
	s_addc_u32 s5, s9, 0
	v_cmp_eq_u32_e32 vcc, 0, v1
	s_and_saveexec_b64 s[8:9], vcc
	s_cbranch_execz .LBB0_994
	s_bcnt1_i32_b64 s6, s[6:7]
	v_mov_b32_e32 v3, 0x1000
	v_mov_b32_e32 v4, s6
	global_atomic_add v3, v3, v4, s[4:5] offset:1024 sc0
	buffer_inv sc1

.Lxb_done_9:
	s_waitcnt vmcnt(0)
.LBB0_1029:
	s_or_b64 exec, exec, s[2:3]
	s_waitcnt lgkmcnt(0)
	s_barrier

.Lxb_done_10:
	s_waitcnt vmcnt(0)
.LBB0_1168:
	s_or_b64 exec, exec, s[0:1]
	v_readlane_b32 s0, v235, 16
	v_readlane_b32 s1, v235, 17
	s_cmpk_lt_i32 s0, 0x200
	v_readlane_b32 s0, v235, 14
	v_readlane_b32 s1, v235, 15
	v_mov_b32_e32 v8, v186
	s_waitcnt lgkmcnt(0)
	s_barrier
	s_nop 0
	v_readfirstlane_b32 s14, v8
	s_cbranch_scc0 .LBB0_1188
	v_lshlrev_b32_e32 v0, 4, v8
	v_add_u32_e32 v1, 0x2000, v0
	v_ashrrev_i32_e32 v2, 31, v1
	v_lshrrev_b32_e32 v2, 22, v2
	v_add_u32_e32 v2, v1, v2
	v_ashrrev_i32_e32 v10, 10, v2
	v_lshlrev_b32_e32 v2, 5, v10
	v_and_b32_e32 v9, 32, v2
	v_mul_i32_i24_e32 v2, 0x400, v10
	v_sub_u32_e32 v1, v1, v2
	v_lshrrev_b32_e32 v2, 4, v1
	v_bitop3_b32 v1, v2, v1, 32 bitop3:0x6c
	v_ashrrev_i32_e32 v2, 31, v1
	v_lshrrev_b32_e32 v2, 26, v2
	v_add_u32_e32 v2, v1, v2
	v_ashrrev_i32_e32 v12, 6, v2
	v_and_b32_e32 v2, 0xc0, v2
	v_lshlrev_b32_e32 v3, 3, v10
	v_sub_u32_e32 v1, v1, v2
	v_mov_b32_e32 v2, 1
	v_and_b32_e32 v3, -16, v3
	v_ashrrev_i16_sdwa v11, v2, sext(v1) dst_sel:DWORD dst_unused:UNUSED_PAD src0_sel:DWORD src1_sel:BYTE_0
	v_add_u32_e32 v3, v12, v3
	s_movk_i32 s16, 0x580
	v_add_u32_sdwa v1, v9, sext(v11) dst_sel:DWORD dst_unused:UNUSED_PAD src0_sel:DWORD src1_sel:WORD_0
	v_mul_lo_u32 v4, v3, s16
	v_add_lshl_u32 v160, v1, v4, 1
	v_ashrrev_i32_e32 v4, 31, v8
	v_lshrrev_b32_e32 v4, 26, v4
	v_add_u32_e32 v4, v8, v4
	v_ashrrev_i32_e32 v14, 6, v4
	v_lshlrev_b32_e32 v4, 5, v14
	v_and_b32_e32 v13, 32, v4
	v_bfe_i32 v4, v8, 27, 1
	v_lshrrev_b32_e32 v4, 22, v4
	v_add_u32_e32 v4, v0, v4
	v_and_b32_e32 v4, 0xfffffc00, v4
	v_sub_u32_e32 v0, v0, v4
	v_lshrrev_b32_e32 v4, 4, v0
	v_bitop3_b32 v4, v4, v0, 32 bitop3:0x6c
	v_ashrrev_i32_e32 v0, 31, v0
	v_lshrrev_b32_e32 v0, 26, v0
	v_add_u32_e32 v0, v4, v0
	v_ashrrev_i32_e32 v16, 6, v0
	v_mul_i32_i24_e32 v0, 64, v16
	v_sub_u32_e32 v0, v4, v0
	v_ashrrev_i16_sdwa v15, v2, sext(v0) dst_sel:DWORD dst_unused:UNUSED_PAD src0_sel:DWORD src1_sel:BYTE_0
	v_lshlrev_b32_e32 v2, 3, v14
	v_and_b32_e32 v2, -16, v2
	s_load_dwordx2 s[6:7], s[0:1], 0x98
	v_add_u32_e32 v2, v16, v2
	v_add_u32_sdwa v0, v13, sext(v15) dst_sel:DWORD dst_unused:UNUSED_PAD src0_sel:DWORD src1_sel:WORD_0
	v_mul_lo_u32 v4, v2, s16
	v_add_lshl_u32 v164, v0, v4, 1
	v_and_b32_e32 v4, 3, v12
	s_mov_b32 s2, 0x1ffffe0
	s_lshl_b32 s0, s47, 3
	v_and_or_b32 v4, v3, s2, v4
	v_lshrrev_b32_e32 v5, 2, v3
	v_lshlrev_b32_e32 v3, 1, v3
	s_or_b32 s59, s0, s46
	v_and_b32_e32 v5, 4, v5
	v_and_b32_e32 v3, 24, v3
	s_waitcnt lgkmcnt(0)
	s_add_u32 s23, s6, 0x11173000
	v_or3_b32 v3, v4, v5, v3
	s_addc_u32 s33, s7, 0
	v_mul_lo_u32 v3, v3, s16
	s_add_u32 s36, s6, 0x7373000
	v_add_lshl_u32 v168, v3, v1, 1
	v_and_b32_e32 v1, 3, v16
	s_addc_u32 s37, s7, 0
	s_ashr_i32 s12, s14, 6
	v_and_or_b32 v1, v2, s2, v1
	v_lshrrev_b32_e32 v3, 2, v2
	v_lshlrev_b32_e32 v2, 1, v2
	s_ashr_i32 s15, s14, 8
	s_lshl_b32 s38, s12, 10
	s_mul_i32 s0, s22, 0xb0000
	v_and_b32_e32 v3, 4, v3
	v_and_b32_e32 v2, 24, v2
	s_mul_hi_i32 s1, s22, 0xb0000
	v_or3_b32 v1, v1, v3, v2
	s_add_u32 s0, s36, s0
	v_mul_lo_u32 v1, v1, s16
	s_addc_u32 s1, s37, s1
	s_add_i32 s39, s38, 0
	v_add_lshl_u32 v170, v1, v0, 1
	v_mov_b32_e32 v188, 0x79797979
	v_mov_b32_e32 v189, 0x7c7c7c7c
	s_add_i32 m0, s39, 0x10000
	s_mul_i32 s5, s59, 0xb0000
	global_load_lds_dwordx4 v170, s[0:1]
	s_add_i32 m0, s39, 0x12000
	s_add_u32 s2, s0, 0x58000
	global_load_lds_dwordx4 v168, s[0:1]
	s_addc_u32 s3, s1, 0
	s_add_i32 m0, s39, 0x14000
	s_mul_hi_i32 s4, s59, 0xb0000
	global_load_lds_dwordx4 v170, s[2:3]
	s_add_i32 m0, s39, 0x16000
	s_add_u32 s28, s23, s5
	global_load_lds_dwordx4 v168, s[2:3]
	s_addc_u32 s29, s33, s4
	s_mov_b32 m0, s39
	s_add_i32 s40, s39, 0x2000
	global_load_lds_dwordx4 v164, s[28:29]
	s_mov_b32 m0, s40
	s_add_i32 s41, s39, 0x4000
	v_add_u32_e32 v166, 0x58000, v164
	global_load_lds_dwordx4 v160, s[28:29]
	s_mov_b32 m0, s41
	s_add_i32 s42, s39, 0x6000
	v_add_u32_e32 v162, 0x58000, v160
	global_load_lds_dwordx4 v166, s[28:29]
	s_mov_b32 m0, s42
	v_mov_b32_e32 v173, 0
	global_load_lds_dwordx4 v162, s[28:29]
	v_mov_b32_e32 v171, v173
	v_mov_b32_e32 v169, v173
	v_mov_b32_e32 v165, v173
	v_mov_b32_e32 v161, v173
	s_cmp_eq_u32 s15, 1
	s_mov_b32 s43, 0x58000
	s_mov_b32 s44, 0
	v_lshl_add_u64 v[6:7], s[0:1], 0, v[170:171]
	v_lshl_add_u64 v[2:3], s[0:1], 0, v[168:169]
	s_mov_b64 s[2:3], 0x58000
	v_lshl_add_u64 v[0:1], s[28:29], 0, v[164:165]
	s_cselect_b64 s[4:5], -1, 0
	s_cmp_lg_u32 s15, 1
	v_lshl_add_u64 v[4:5], s[28:29], 0, v[160:161]
	s_cbranch_scc1 .LBB0_1171
	s_barrier

.Lxb_done_11:
	s_waitcnt vmcnt(0)
.LBB0_1241:
	s_or_b64 exec, exec, s[0:1]
	s_waitcnt lgkmcnt(0)
	s_barrier
	v_readlane_b32 s0, v235, 18
	v_ashrrev_i32_e32 v0, 5, v186
	v_and_b32_e32 v0, -2, v0
	v_add_u32_e32 v16, s0, v0
	s_movk_i32 s0, 0x4000
	v_cmp_gt_i32_e32 vcc, s0, v16
	s_and_saveexec_b64 s[0:1], vcc
	s_cbranch_execz .LBB0_1250
	s_load_dwordx2 s[4:5], s[46:47], 0x98
	s_load_dwordx4 s[0:3], s[46:47], 0x88
	v_and_b32_e32 v0, 31, v186
	v_mov_b32_e32 v19, 0
	v_lshlrev_b32_e32 v18, 2, v0
	s_waitcnt lgkmcnt(0)
	v_lshl_add_u64 v[0:1], s[4:5], 0, v[18:19]
	s_mov_b64 s[6:7], 0x15b000
	v_lshl_add_u64 v[20:21], v[0:1], 0, s[6:7]
	v_lshlrev_b32_e32 v0, 3, v186
	v_and_b32_e32 v0, 0x1f8, v0
	v_lshlrev_b32_e32 v18, 1, v0
	v_lshl_add_u64 v[2:3], s[4:5], 0, v[18:19]
	s_mov_b64 s[6:7], 0x9f73000
	v_lshl_add_u64 v[22:23], v[2:3], 0, s[6:7]
	s_mov_b64 s[6:7], 0x1b73000
	v_mbcnt_hi_u32_b32 v1, -1, v187
	v_lshl_add_u64 v[24:25], v[2:3], 0, s[6:7]
	v_and_b32_e32 v2, 64, v1
	v_add_u32_e32 v2, 64, v2
	v_xor_b32_e32 v3, 32, v1
	v_cmp_lt_i32_e32 vcc, v3, v2
	v_lshlrev_b32_e32 v18, 2, v0
	v_lshl_add_u64 v[26:27], s[0:1], 0, v[18:19]
	v_cndmask_b32_e32 v3, v1, v3, vcc
	v_lshlrev_b32_e32 v66, 2, v3
	v_xor_b32_e32 v3, 16, v1
	v_cmp_lt_i32_e32 vcc, v3, v2
	v_lshl_add_u64 v[28:29], s[2:3], 0, v[18:19]
	s_mov_b64 s[0:1], 0
	v_cndmask_b32_e32 v3, v1, v3, vcc
	v_lshlrev_b32_e32 v67, 2, v3
	v_xor_b32_e32 v3, 8, v1
	v_cmp_lt_i32_e32 vcc, v3, v2
	v_lshlrev_b32_e32 v18, 2, v0
	s_mov_b64 s[2:3], 0x5000
	v_cndmask_b32_e32 v3, v1, v3, vcc
	v_lshlrev_b32_e32 v68, 2, v3
	v_xor_b32_e32 v3, 4, v1
	v_cmp_lt_i32_e32 vcc, v3, v2
	s_movk_i32 s6, 0x5000
	v_mov_b32_e32 v72, 0x358637bd
	v_cndmask_b32_e32 v3, v1, v3, vcc
	v_lshlrev_b32_e32 v69, 2, v3
	v_xor_b32_e32 v3, 2, v1
	v_cmp_lt_i32_e32 vcc, v3, v2
	s_mov_b32 s7, 0x800000
	s_movk_i32 s8, 0x3fff
	v_cndmask_b32_e32 v3, v1, v3, vcc
	v_lshlrev_b32_e32 v70, 2, v3
	v_xor_b32_e32 v3, 1, v1
	v_cmp_lt_i32_e32 vcc, v3, v2
	s_nop 1
	v_cndmask_b32_e32 v1, v1, v3, vcc
	v_lshlrev_b32_e32 v71, 2, v1
	s_branch .LBB0_1244

	.amdhsa_kernel _Z4mega6Params
		.amdhsa_group_segment_fixed_size 0
		.amdhsa_private_segment_fixed_size 0
		.amdhsa_kernarg_size 416
		.amdhsa_user_sgpr_count 2
		.amdhsa_user_sgpr_dispatch_ptr 0
		.amdhsa_user_sgpr_queue_ptr 0
		.amdhsa_user_sgpr_kernarg_segment_ptr 1
		.amdhsa_user_sgpr_dispatch_id 0
		.amdhsa_user_sgpr_kernarg_preload_length 0
		.amdhsa_user_sgpr_kernarg_preload_offset 0
		.amdhsa_user_sgpr_private_segment_size 0
		.amdhsa_uses_dynamic_stack 0
		.amdhsa_enable_private_segment 0
		.amdhsa_system_sgpr_workgroup_id_x 1
		.amdhsa_system_sgpr_workgroup_id_y 0
		.amdhsa_system_sgpr_workgroup_id_z 0
		.amdhsa_system_sgpr_workgroup_info 0
		.amdhsa_system_vgpr_workitem_id 2
		.amdhsa_next_free_vgpr 240
		.amdhsa_next_free_sgpr 102
		.amdhsa_accum_offset 240
		.amdhsa_reserve_vcc 1
		.amdhsa_float_round_mode_32 0
		.amdhsa_float_round_mode_16_64 0
		.amdhsa_float_denorm_mode_32 3
		.amdhsa_float_denorm_mode_16_64 3
		.amdhsa_dx10_clamp 1
		.amdhsa_ieee_mode 1
		.amdhsa_fp16_overflow 0
		.amdhsa_tg_split 0
		.amdhsa_exception_fp_ieee_invalid_op 0
		.amdhsa_exception_fp_denorm_src 0
		.amdhsa_exception_fp_ieee_div_zero 0
		.amdhsa_exception_fp_ieee_overflow 0
		.amdhsa_exception_fp_ieee_underflow 0
		.amdhsa_exception_fp_ieee_inexact 0
		.amdhsa_exception_int_div_zero 0
	.end_amdhsa_kernel

amdhsa.kernels:
  - .agpr_count:     0
    .args:
      - .offset:         0
        .size:           160
        .value_kind:     by_value
      - .offset:         160
        .size:           4
        .value_kind:     hidden_block_count_x
      - .offset:         164
        .size:           4
        .value_kind:     hidden_block_count_y
      - .offset:         168
        .size:           4
        .value_kind:     hidden_block_count_z
      - .offset:         172
        .size:           2
        .value_kind:     hidden_group_size_x
      - .offset:         174
        .size:           2
        .value_kind:     hidden_group_size_y
      - .offset:         176
        .size:           2
        .value_kind:     hidden_group_size_z
      - .offset:         178
        .size:           2
        .value_kind:     hidden_remainder_x
      - .offset:         180
        .size:           2
        .value_kind:     hidden_remainder_y
      - .offset:         182
        .size:           2
        .value_kind:     hidden_remainder_z
      - .offset:         200
        .size:           8
        .value_kind:     hidden_global_offset_x
      - .offset:         208
        .size:           8
        .value_kind:     hidden_global_offset_y
      - .offset:         216
        .size:           8
        .value_kind:     hidden_global_offset_z
      - .offset:         224
        .size:           2
        .value_kind:     hidden_grid_dims
      - .offset:         248
        .size:           8
        .value_kind:     hidden_multigrid_sync_arg
      - .offset:         280
        .size:           4
        .value_kind:     hidden_dynamic_lds_size
    .group_segment_fixed_size: 0
    .kernarg_segment_align: 8
    .kernarg_segment_size: 416
    .language:       OpenCL C
    .language_version:
      - 2
      - 0
    .max_flat_workgroup_size: 512
    .name:           _Z4mega6Params
    .private_segment_fixed_size: 0
    .sgpr_count:     108
    .sgpr_spill_count: 48
    .symbol:         _Z4mega6Params.kd
    .uniform_work_group_size: 1
    .uses_dynamic_stack: false
    .vgpr_count:     240
    .vgpr_spill_count: 0
    .wavefront_size: 64
